# P8 router-logit MFMA loop: cross-iteration prefetch with two register sets (next trip's 20 loads issued before the current trip's 16 f32 MFMAs)
# speedup vs baseline: 1.0044x; 1.0006x over previous
; #define UNP4(v) ((f32x4){__uint_as_float((v).x << 16), __uint_as_float((v).x & 0xffff0000u), __uint_as_float((v).y << 16), __uint_as_float((v).y & 0xffff0000u)})
; __device__ __forceinline__ void p8_route(Frame& F) {
;     ...
;         float ss = 0.f; const float* bp = RWS + (size_t)(256 * w + 4 * h) * NE + i;
; #pragma unroll 4
;         for (int q = 0; q < 32; ++q) { const v2u xb_ = *(const v2u*)(xrow + 8 * q); const f32x4 xa = UNP4(xb_);
; #pragma unroll
;             for (int j = 0; j < 4; ++j) acc = __builtin_amdgcn_mfma_f32_32x32x2f32(xa[j], bp[(8 * q + j) * NE], acc, 0, 0, 0);
;             ss += (xa[0] * xa[0] + xa[1] * xa[1]) + (xa[2] * xa[2] + xa[3] * xa[3]); }
.LBB0_1427:
	s_mov_b32 s10, 4
	v_lshl_add_u64 v[40:41], s[90:91], 0, v[36:37]
	v_lshl_add_u64 v[42:43], s[90:91], 0, v[38:39]
	v_add_co_u32_e32 v42, vcc, s26, v42
	s_nop 1
	v_addc_co_u32_e32 v43, vcc, 0, v43, vcc
	global_load_dwordx2 v[76:77], v[40:41], off offset:-32
	global_load_dwordx2 v[78:79], v[40:41], off offset:-16
	global_load_dwordx2 v[80:81], v[40:41], off
	global_load_dwordx2 v[82:83], v[40:41], off offset:16
	global_load_dword v84, v[42:43], off
	global_load_dword v85, v[42:43], off offset:128
	global_load_dword v86, v[42:43], off offset:256
	global_load_dword v87, v[42:43], off offset:384
	global_load_dword v88, v[42:43], off offset:1024
	global_load_dword v89, v[42:43], off offset:1152
	global_load_dword v90, v[42:43], off offset:1280
	global_load_dword v91, v[42:43], off offset:1408
	global_load_dword v92, v[42:43], off offset:2048
	global_load_dword v93, v[42:43], off offset:2176
	global_load_dword v94, v[42:43], off offset:2304
	global_load_dword v95, v[42:43], off offset:2432
	global_load_dword v96, v[42:43], off offset:3072
	global_load_dword v97, v[42:43], off offset:3200
	global_load_dword v98, v[42:43], off offset:3328
	global_load_dword v99, v[42:43], off offset:3456
	v_lshl_add_u64 v[38:39], v[38:39], 0, s[18:19]
	v_lshl_add_u64 v[36:37], v[36:37], 0, 64
.Lp8_mm_loop:
	v_lshl_add_u64 v[124:125], s[90:91], 0, v[36:37]
	v_lshl_add_u64 v[126:127], s[90:91], 0, v[38:39]
	v_add_co_u32_e32 v126, vcc, s26, v126
	s_nop 1
	v_addc_co_u32_e32 v127, vcc, 0, v127, vcc
	global_load_dwordx2 v[100:101], v[124:125], off offset:-32
	global_load_dwordx2 v[102:103], v[124:125], off offset:-16
	global_load_dwordx2 v[104:105], v[124:125], off
	global_load_dwordx2 v[106:107], v[124:125], off offset:16
	global_load_dword v108, v[126:127], off
	global_load_dword v109, v[126:127], off offset:128
	global_load_dword v110, v[126:127], off offset:256
	global_load_dword v111, v[126:127], off offset:384
	global_load_dword v112, v[126:127], off offset:1024
	global_load_dword v113, v[126:127], off offset:1152
	global_load_dword v114, v[126:127], off offset:1280
	global_load_dword v115, v[126:127], off offset:1408
	global_load_dword v116, v[126:127], off offset:2048
	global_load_dword v117, v[126:127], off offset:2176
	global_load_dword v118, v[126:127], off offset:2304
	global_load_dword v119, v[126:127], off offset:2432
	global_load_dword v120, v[126:127], off offset:3072
	global_load_dword v121, v[126:127], off offset:3200
	global_load_dword v122, v[126:127], off offset:3328
	global_load_dword v123, v[126:127], off offset:3456
	v_lshl_add_u64 v[38:39], v[38:39], 0, s[18:19]
	v_lshl_add_u64 v[36:37], v[36:37], 0, 64
	s_waitcnt vmcnt(20)
	v_lshlrev_b32_e32 v62, 16, v76
	v_and_b32_e32 v76, 0xffff0000, v76
	v_lshlrev_b32_e32 v63, 16, v77
	v_and_b32_e32 v77, 0xffff0000, v77
	v_mfma_f32_32x32x2_f32 v[2:17], v62, v84, v[2:17]
	v_lshlrev_b32_e32 v64, 16, v78
	v_and_b32_e32 v78, 0xffff0000, v78
	v_lshlrev_b32_e32 v65, 16, v79
	v_and_b32_e32 v79, 0xffff0000, v79
	v_mfma_f32_32x32x2_f32 v[2:17], v76, v85, v[2:17]
	v_mfma_f32_32x32x2_f32 v[2:17], v63, v86, v[2:17]
	v_mfma_f32_32x32x2_f32 v[2:17], v77, v87, v[2:17]
	v_mul_f32_e64 v76, v76, v76
	v_mul_f32_e64 v77, v77, v77
	v_fma_f32 v76, v62, v62, v76
	v_fma_f32 v77, v63, v63, v77
	v_add_f32_e32 v76, v76, v77
	v_add_f32_e32 v18, v18, v76
	v_mfma_f32_32x32x2_f32 v[2:17], v64, v88, v[2:17]
	v_lshlrev_b32_e32 v62, 16, v80
	v_and_b32_e32 v80, 0xffff0000, v80
	v_lshlrev_b32_e32 v63, 16, v81
	v_and_b32_e32 v81, 0xffff0000, v81
	v_mfma_f32_32x32x2_f32 v[2:17], v78, v89, v[2:17]
	v_mfma_f32_32x32x2_f32 v[2:17], v65, v90, v[2:17]
	v_mfma_f32_32x32x2_f32 v[2:17], v79, v91, v[2:17]
	v_mul_f32_e64 v78, v78, v78
	v_mul_f32_e64 v79, v79, v79
	v_fma_f32 v78, v64, v64, v78
	v_fma_f32 v79, v65, v65, v79
	v_add_f32_e32 v78, v78, v79
	v_add_f32_e32 v18, v18, v78
	v_mfma_f32_32x32x2_f32 v[2:17], v62, v92, v[2:17]
	v_lshlrev_b32_e32 v64, 16, v82
	v_and_b32_e32 v82, 0xffff0000, v82
	v_lshlrev_b32_e32 v65, 16, v83
	v_and_b32_e32 v83, 0xffff0000, v83
	v_mfma_f32_32x32x2_f32 v[2:17], v80, v93, v[2:17]
	v_mfma_f32_32x32x2_f32 v[2:17], v63, v94, v[2:17]
	v_mfma_f32_32x32x2_f32 v[2:17], v81, v95, v[2:17]
	v_mul_f32_e64 v80, v80, v80
	v_mul_f32_e64 v81, v81, v81
	v_fma_f32 v80, v62, v62, v80
	v_fma_f32 v81, v63, v63, v81
	v_add_f32_e32 v80, v80, v81
	v_add_f32_e32 v18, v18, v80
	v_mfma_f32_32x32x2_f32 v[2:17], v64, v96, v[2:17]
	v_mfma_f32_32x32x2_f32 v[2:17], v82, v97, v[2:17]
	v_mfma_f32_32x32x2_f32 v[2:17], v65, v98, v[2:17]
	v_mfma_f32_32x32x2_f32 v[2:17], v83, v99, v[2:17]
	v_mul_f32_e64 v82, v82, v82
	v_mul_f32_e64 v83, v83, v83
	v_fma_f32 v82, v64, v64, v82
	v_fma_f32 v83, v65, v65, v83
	v_add_f32_e32 v82, v82, v83
	v_add_f32_e32 v18, v18, v82
	s_add_i32 s10, s10, -1
	s_cmp_eq_u32 s10, 0
	s_cbranch_scc1 .Lp8_mm_last
; #define UNP4(v) ((f32x4){__uint_as_float((v).x << 16), __uint_as_float((v).x & 0xffff0000u), __uint_as_float((v).y << 16), __uint_as_float((v).y & 0xffff0000u)})
; __device__ __forceinline__ void p8_route(Frame& F) {
;     ...
;         float ss = 0.f; const float* bp = RWS + (size_t)(256 * w + 4 * h) * NE + i;
; #pragma unroll 4
;         for (int q = 0; q < 32; ++q) { const v2u xb_ = *(const v2u*)(xrow + 8 * q); const f32x4 xa = UNP4(xb_);
; #pragma unroll
;             for (int j = 0; j < 4; ++j) acc = __builtin_amdgcn_mfma_f32_32x32x2f32(xa[j], bp[(8 * q + j) * NE], acc, 0, 0, 0);
;             ss += (xa[0] * xa[0] + xa[1] * xa[1]) + (xa[2] * xa[2] + xa[3] * xa[3]); }
;         ss += __shfl_xor(ss, 32);
;         if (h == 0) ssq[w * 32 + i] = ss;
	v_lshl_add_u64 v[40:41], s[90:91], 0, v[36:37]
	v_lshl_add_u64 v[42:43], s[90:91], 0, v[38:39]
	v_add_co_u32_e32 v42, vcc, s26, v42
	s_nop 1
	v_addc_co_u32_e32 v43, vcc, 0, v43, vcc
	global_load_dwordx2 v[76:77], v[40:41], off offset:-32
	global_load_dwordx2 v[78:79], v[40:41], off offset:-16
	global_load_dwordx2 v[80:81], v[40:41], off
	global_load_dwordx2 v[82:83], v[40:41], off offset:16
	global_load_dword v84, v[42:43], off
	global_load_dword v85, v[42:43], off offset:128
	global_load_dword v86, v[42:43], off offset:256
	global_load_dword v87, v[42:43], off offset:384
	global_load_dword v88, v[42:43], off offset:1024
	global_load_dword v89, v[42:43], off offset:1152
	global_load_dword v90, v[42:43], off offset:1280
	global_load_dword v91, v[42:43], off offset:1408
	global_load_dword v92, v[42:43], off offset:2048
	global_load_dword v93, v[42:43], off offset:2176
	global_load_dword v94, v[42:43], off offset:2304
	global_load_dword v95, v[42:43], off offset:2432
	global_load_dword v96, v[42:43], off offset:3072
	global_load_dword v97, v[42:43], off offset:3200
	global_load_dword v98, v[42:43], off offset:3328
	global_load_dword v99, v[42:43], off offset:3456
	v_lshl_add_u64 v[38:39], v[38:39], 0, s[18:19]
	v_lshl_add_u64 v[36:37], v[36:37], 0, 64
	s_waitcnt vmcnt(20)
	v_lshlrev_b32_e32 v62, 16, v100
	v_and_b32_e32 v100, 0xffff0000, v100
	v_lshlrev_b32_e32 v63, 16, v101
	v_and_b32_e32 v101, 0xffff0000, v101
	v_mfma_f32_32x32x2_f32 v[2:17], v62, v108, v[2:17]
	v_lshlrev_b32_e32 v64, 16, v102
	v_and_b32_e32 v102, 0xffff0000, v102
	v_lshlrev_b32_e32 v65, 16, v103
	v_and_b32_e32 v103, 0xffff0000, v103
	v_mfma_f32_32x32x2_f32 v[2:17], v100, v109, v[2:17]
	v_mfma_f32_32x32x2_f32 v[2:17], v63, v110, v[2:17]
	v_mfma_f32_32x32x2_f32 v[2:17], v101, v111, v[2:17]
	v_mul_f32_e64 v100, v100, v100
	v_mul_f32_e64 v101, v101, v101
	v_fma_f32 v100, v62, v62, v100
	v_fma_f32 v101, v63, v63, v101
	v_add_f32_e32 v100, v100, v101
	v_add_f32_e32 v18, v18, v100
	v_mfma_f32_32x32x2_f32 v[2:17], v64, v112, v[2:17]
	v_lshlrev_b32_e32 v62, 16, v104
	v_and_b32_e32 v104, 0xffff0000, v104
	v_lshlrev_b32_e32 v63, 16, v105
	v_and_b32_e32 v105, 0xffff0000, v105
	v_mfma_f32_32x32x2_f32 v[2:17], v102, v113, v[2:17]
	v_mfma_f32_32x32x2_f32 v[2:17], v65, v114, v[2:17]
	v_mfma_f32_32x32x2_f32 v[2:17], v103, v115, v[2:17]
	v_mul_f32_e64 v102, v102, v102
	v_mul_f32_e64 v103, v103, v103
	v_fma_f32 v102, v64, v64, v102
	v_fma_f32 v103, v65, v65, v103
	v_add_f32_e32 v102, v102, v103
	v_add_f32_e32 v18, v18, v102
	v_mfma_f32_32x32x2_f32 v[2:17], v62, v116, v[2:17]
	v_lshlrev_b32_e32 v64, 16, v106
	v_and_b32_e32 v106, 0xffff0000, v106
	v_lshlrev_b32_e32 v65, 16, v107
	v_and_b32_e32 v107, 0xffff0000, v107
	v_mfma_f32_32x32x2_f32 v[2:17], v104, v117, v[2:17]
	v_mfma_f32_32x32x2_f32 v[2:17], v63, v118, v[2:17]
	v_mfma_f32_32x32x2_f32 v[2:17], v105, v119, v[2:17]
	v_mul_f32_e64 v104, v104, v104
	v_mul_f32_e64 v105, v105, v105
	v_fma_f32 v104, v62, v62, v104
	v_fma_f32 v105, v63, v63, v105
	v_add_f32_e32 v104, v104, v105
	v_add_f32_e32 v18, v18, v104
	v_mfma_f32_32x32x2_f32 v[2:17], v64, v120, v[2:17]
	v_mfma_f32_32x32x2_f32 v[2:17], v106, v121, v[2:17]
	v_mfma_f32_32x32x2_f32 v[2:17], v65, v122, v[2:17]
	v_mfma_f32_32x32x2_f32 v[2:17], v107, v123, v[2:17]
	v_mul_f32_e64 v106, v106, v106
	v_mul_f32_e64 v107, v107, v107
	v_fma_f32 v106, v64, v64, v106
	v_fma_f32 v107, v65, v65, v107
	v_add_f32_e32 v106, v106, v107
	v_add_f32_e32 v18, v18, v106
	s_branch .Lp8_mm_loop
.Lp8_mm_last:
	s_waitcnt vmcnt(0)
	v_lshlrev_b32_e32 v62, 16, v100
	v_and_b32_e32 v100, 0xffff0000, v100
	v_lshlrev_b32_e32 v63, 16, v101
	v_and_b32_e32 v101, 0xffff0000, v101
	v_mfma_f32_32x32x2_f32 v[2:17], v62, v108, v[2:17]
	v_lshlrev_b32_e32 v64, 16, v102
	v_and_b32_e32 v102, 0xffff0000, v102
	v_lshlrev_b32_e32 v65, 16, v103
	v_and_b32_e32 v103, 0xffff0000, v103
	v_mfma_f32_32x32x2_f32 v[2:17], v100, v109, v[2:17]
	v_mfma_f32_32x32x2_f32 v[2:17], v63, v110, v[2:17]
	v_mfma_f32_32x32x2_f32 v[2:17], v101, v111, v[2:17]
	v_mul_f32_e64 v100, v100, v100
	v_mul_f32_e64 v101, v101, v101
	v_fma_f32 v100, v62, v62, v100
	v_fma_f32 v101, v63, v63, v101
	v_add_f32_e32 v100, v100, v101
	v_add_f32_e32 v18, v18, v100
	v_mfma_f32_32x32x2_f32 v[2:17], v64, v112, v[2:17]
	v_lshlrev_b32_e32 v62, 16, v104
	v_and_b32_e32 v104, 0xffff0000, v104
	v_lshlrev_b32_e32 v63, 16, v105
	v_and_b32_e32 v105, 0xffff0000, v105
	v_mfma_f32_32x32x2_f32 v[2:17], v102, v113, v[2:17]
	v_mfma_f32_32x32x2_f32 v[2:17], v65, v114, v[2:17]
	v_mfma_f32_32x32x2_f32 v[2:17], v103, v115, v[2:17]
	v_mul_f32_e64 v102, v102, v102
	v_mul_f32_e64 v103, v103, v103
	v_fma_f32 v102, v64, v64, v102
	v_fma_f32 v103, v65, v65, v103
	v_add_f32_e32 v102, v102, v103
	v_add_f32_e32 v18, v18, v102
	v_mfma_f32_32x32x2_f32 v[2:17], v62, v116, v[2:17]
	v_lshlrev_b32_e32 v64, 16, v106
	v_and_b32_e32 v106, 0xffff0000, v106
	v_lshlrev_b32_e32 v65, 16, v107
	v_and_b32_e32 v107, 0xffff0000, v107
	v_mfma_f32_32x32x2_f32 v[2:17], v104, v117, v[2:17]
	v_mfma_f32_32x32x2_f32 v[2:17], v63, v118, v[2:17]
	v_mfma_f32_32x32x2_f32 v[2:17], v105, v119, v[2:17]
	v_mul_f32_e64 v104, v104, v104
	v_mul_f32_e64 v105, v105, v105
	v_fma_f32 v104, v62, v62, v104
	v_fma_f32 v105, v63, v63, v105
	v_add_f32_e32 v104, v104, v105
	v_add_f32_e32 v18, v18, v104
	v_mfma_f32_32x32x2_f32 v[2:17], v64, v120, v[2:17]
	v_mfma_f32_32x32x2_f32 v[2:17], v106, v121, v[2:17]
	v_mfma_f32_32x32x2_f32 v[2:17], v65, v122, v[2:17]
	v_mfma_f32_32x32x2_f32 v[2:17], v107, v123, v[2:17]
	v_mul_f32_e64 v106, v106, v106
	v_mul_f32_e64 v107, v107, v107
	v_fma_f32 v106, v64, v64, v106
	v_fma_f32 v107, v65, v65, v107
	v_add_f32_e32 v106, v106, v107
	v_add_f32_e32 v18, v18, v106
	s_nop 1
	ds_bpermute_b32 v36, v1, v18
	s_and_saveexec_b64 s[10:11], s[4:5]
	s_cbranch_execz .LBB0_1430
	s_waitcnt lgkmcnt(0)
	v_add_f32_e32 v18, v18, v36
	ds_write_b32 v53, v18 offset:33792
